# baseline (speedup 1.0000x reference)
.LBB1_100:
	s_or_b64 exec, exec, s[6:7]
	s_waitcnt vmcnt(1)
	v_sub_u32_e32 v8, 0, v4
	v_max_i32_e32 v8, v4, v8
	v_cvt_f32_u32_e32 v9, v8
	v_sub_u32_e32 v12, 0, v8
	v_sub_u32_e32 v1, v1, v20
	v_sub_u32_e32 v11, 0, v1
	v_rcp_iflag_f32_e32 v9, v9
	v_max_i32_e32 v11, v1, v11
	v_xor_b32_e32 v10, v1, v4
	v_ashrrev_i32_e32 v10, 31, v10
	v_mul_f32_e32 v9, 0x4f7ffffe, v9
	v_cvt_u32_f32_e32 v9, v9
	v_mul_lo_u32 v12, v12, v9
	v_mul_hi_u32 v12, v9, v12
	v_add_u32_e32 v9, v9, v12
	v_mul_hi_u32 v9, v11, v9
	v_mul_lo_u32 v12, v9, v8
	v_sub_u32_e32 v11, v11, v12
	v_add_u32_e32 v13, 1, v9
	v_cmp_ge_u32_e32 vcc, v11, v8
	v_sub_u32_e32 v12, v11, v8
	s_nop 0
	v_cndmask_b32_e32 v9, v9, v13, vcc
	v_cndmask_b32_e32 v11, v11, v12, vcc
	v_add_u32_e32 v12, 1, v9
	v_cmp_ge_u32_e32 vcc, v11, v8
	s_nop 1
	v_cndmask_b32_e32 v8, v9, v12, vcc
	v_xor_b32_e32 v8, v8, v10
	v_sub_u32_e32 v9, v8, v10
	v_mul_lo_u32 v8, v9, v4
	v_lshrrev_b32_e32 v10, 1, v0
	v_sub_u32_e32 v8, v1, v8
	v_and_b32_e32 v10, 24, v10
	v_lshl_or_b32 v18, v8, 5, v10
	v_lshlrev_b32_e32 v10, 4, v9
	v_and_b32_e32 v1, 15, v0
	v_ashrrev_i32_e32 v11, 31, v10
	v_lshl_add_u64 v[6:7], v[10:11], 2, v[6:7]
	v_lshlrev_b32_e32 v10, 2, v1
	v_or_b32_e32 v1, 1, v18
	v_mad_i64_i32 v[14:15], s[6:7], v1, v19, 0
	v_or_b32_e32 v1, 2, v18
	v_mad_i64_i32 v[16:17], s[6:7], v1, v19, 0
	v_or_b32_e32 v1, 3, v18
	v_mad_i64_i32 v[20:21], s[6:7], v1, v19, 0
	v_or_b32_e32 v1, 4, v18
	v_mad_i64_i32 v[22:23], s[6:7], v1, v19, 0
	v_or_b32_e32 v1, 5, v18
	v_mov_b32_e32 v11, 0
	v_mad_i64_i32 v[24:25], s[6:7], v1, v19, 0
	v_or_b32_e32 v1, 6, v18
	v_lshl_add_u64 v[6:7], v[6:7], 0, v[10:11]
	v_mad_i64_i32 v[12:13], s[6:7], v18, v19, 0
	v_mad_i64_i32 v[26:27], s[6:7], v1, v19, 0
	v_or_b32_e32 v1, 7, v18
	v_lshl_add_u64 v[12:13], v[12:13], 2, v[6:7]
	v_mad_i64_i32 v[18:19], s[6:7], v1, v19, 0
	v_lshl_add_u64 v[14:15], v[14:15], 2, v[6:7]
	v_lshl_add_u64 v[16:17], v[16:17], 2, v[6:7]
	v_lshl_add_u64 v[20:21], v[20:21], 2, v[6:7]
	v_lshl_add_u64 v[22:23], v[22:23], 2, v[6:7]
	v_lshl_add_u64 v[24:25], v[24:25], 2, v[6:7]
	v_lshl_add_u64 v[26:27], v[26:27], 2, v[6:7]
	v_lshl_add_u64 v[6:7], v[18:19], 2, v[6:7]
	global_load_dword v1, v[12:13], off nt
	global_load_dword v18, v[14:15], off nt
	global_load_dword v19, v[16:17], off nt
	global_load_dword v28, v[20:21], off nt
	global_load_dword v29, v[22:23], off nt
	global_load_dword v30, v[24:25], off nt
	global_load_dword v31, v[26:27], off nt
	global_load_dword v32, v[6:7], off nt
	s_waitcnt vmcnt(8)
	v_add_u32_e32 v5, v9, v5
	v_mad_u64_u32 v[4:5], s[6:7], v5, v4, v[8:9]
	v_ashrrev_i32_e32 v5, 31, v4
	v_lshlrev_b32_e32 v6, 4, v0
	v_lshlrev_b64 v[4:5], 10, v[4:5]
	v_and_b32_e32 v10, 0x3f0, v6
	v_lshl_add_u64 v[6:7], v[2:3], 0, v[4:5]
	v_lshl_add_u64 v[6:7], v[6:7], 0, v[10:11]
	s_waitcnt vmcnt(6)
	v_cvt_pk_bf16_f32 v2, v1, v18
	s_waitcnt vmcnt(4)
	v_cvt_pk_bf16_f32 v3, v19, v28
	s_waitcnt vmcnt(2)
	v_cvt_pk_bf16_f32 v4, v29, v30
	s_waitcnt vmcnt(0)
	v_cvt_pk_bf16_f32 v5, v31, v32
	global_store_dwordx4 v[6:7], v[2:5], off

.LBB1_114:
	s_or_b64 exec, exec, s[8:9]
	s_waitcnt vmcnt(0)
	v_sub_u32_e32 v8, 0, v4
	v_max_i32_e32 v8, v4, v8
	v_cvt_f32_u32_e32 v9, v8
	v_sub_u32_e32 v12, 0, v8
	v_sub_u32_e32 v1, v1, v17
	v_sub_u32_e32 v11, 0, v1
	v_rcp_iflag_f32_e32 v9, v9
	v_max_i32_e32 v11, v1, v11
	v_xor_b32_e32 v10, v1, v4
	v_ashrrev_i32_e32 v10, 31, v10
	v_mul_f32_e32 v9, 0x4f7ffffe, v9
	v_cvt_u32_f32_e32 v9, v9
	s_movk_i32 s3, 0x300
	v_mul_lo_u32 v12, v12, v9
	v_mul_hi_u32 v12, v9, v12
	v_add_u32_e32 v9, v9, v12
	v_mul_hi_u32 v9, v11, v9
	v_mul_lo_u32 v12, v9, v8
	v_sub_u32_e32 v11, v11, v12
	v_add_u32_e32 v13, 1, v9
	v_cmp_ge_u32_e32 vcc, v11, v8
	v_sub_u32_e32 v12, v11, v8
	s_nop 0
	v_cndmask_b32_e32 v9, v9, v13, vcc
	v_cndmask_b32_e32 v11, v11, v12, vcc
	v_add_u32_e32 v12, 1, v9
	v_cmp_ge_u32_e32 vcc, v11, v8
	s_nop 1
	v_cndmask_b32_e32 v8, v9, v12, vcc
	v_xor_b32_e32 v8, v8, v10
	v_sub_u32_e32 v9, v8, v10
	v_mul_lo_u32 v8, v9, v4
	v_lshlrev_b32_e32 v10, 3, v9
	v_sub_u32_e32 v8, v1, v8
	v_or_b32_e32 v1, 1, v10
	v_mad_i64_i32 v[14:15], s[4:5], v1, v4, 0
	v_or_b32_e32 v1, 2, v10
	v_mad_i64_i32 v[16:17], s[4:5], v1, v4, 0
	v_or_b32_e32 v1, 3, v10
	v_mad_i64_i32 v[18:19], s[4:5], v1, v4, 0
	v_or_b32_e32 v1, 4, v10
	v_mad_i64_i32 v[20:21], s[4:5], v1, v4, 0
	v_or_b32_e32 v1, 5, v10
	v_ashrrev_i32_e32 v9, 31, v8
	v_mad_i64_i32 v[22:23], s[4:5], v1, v4, 0
	v_or_b32_e32 v1, 6, v10
	v_lshl_add_u64 v[6:7], v[8:9], 2, v[6:7]
	v_mad_i64_i32 v[12:13], s[4:5], v10, v4, 0
	v_mad_i64_i32 v[24:25], s[4:5], v1, v4, 0
	v_or_b32_e32 v1, 7, v10
	v_lshl_add_u64 v[12:13], v[12:13], 2, v[6:7]
	v_mad_i64_i32 v[26:27], s[4:5], v1, v4, 0
	v_lshl_add_u64 v[14:15], v[14:15], 2, v[6:7]
	v_lshl_add_u64 v[16:17], v[16:17], 2, v[6:7]
	v_lshl_add_u64 v[18:19], v[18:19], 2, v[6:7]
	v_lshl_add_u64 v[20:21], v[20:21], 2, v[6:7]
	v_lshl_add_u64 v[22:23], v[22:23], 2, v[6:7]
	v_lshl_add_u64 v[24:25], v[24:25], 2, v[6:7]
	v_lshl_add_u64 v[6:7], v[26:27], 2, v[6:7]
	global_load_dword v1, v[12:13], off nt
	global_load_dword v4, v[14:15], off nt
	global_load_dword v9, v[16:17], off nt
	global_load_dword v26, v[18:19], off nt
	global_load_dword v27, v[20:21], off nt
	global_load_dword v28, v[22:23], off nt
	global_load_dword v29, v[24:25], off nt
	global_load_dword v30, v[6:7], off nt
	v_add_u32_e32 v5, v8, v5
	v_ashrrev_i32_e32 v11, 31, v10
	v_mad_i64_i32 v[6:7], s[4:5], v5, s3, v[2:3]
	v_lshl_add_u64 v[6:7], v[10:11], 1, v[6:7]
	s_waitcnt vmcnt(6)
	v_cvt_pk_bf16_f32 v2, v1, v4
	s_waitcnt vmcnt(4)
	v_cvt_pk_bf16_f32 v3, v9, v26
	s_waitcnt vmcnt(2)
	v_cvt_pk_bf16_f32 v4, v27, v28
	s_waitcnt vmcnt(0)
	v_cvt_pk_bf16_f32 v5, v29, v30
	global_store_dwordx4 v[6:7], v[2:5], off
